# P10: the per-iteration workgroup barrier is skipped in the first iteration of each token (the per-token barrier precedes it by one token prologue)
# speedup vs baseline: 1.0082x; 1.0082x over previous
; __device__ __forceinline__ void expert_tokens(const unsigned char* __restrict__ UV, const float* __restrict__ US, const float* __restrict__ VS, ...
;     ...
; #pragma unroll 1
;         for (int bi = 0; bi < 128 / EB; bi += 2) {
;             EXP_STEP(A, bi);
;             if (bi == 0) { nsu0 = US[ni0]; nsu1 = US[ni1]; nsv0 = VS[ni0]; nsv1 = VS[ni1]; }
;             EXP_STEP(B, bi + 1);
.LBB0_1019:
	s_cmp_eq_u32 s84, 0
	s_cbranch_scc1 .Lp10_nobar_i
	s_cmp_eq_u32 s25, 0
	s_cbranch_scc1 .Lp10_nobar_i
	s_barrier
